# speedup vs baseline: 1.0109x; 1.0104x over previous
.LBB3_13:
	s_or_b64 exec, exec, s[4:5]
	v_mov_b32_e32 v172, 0
	v_ashrrev_i32_e32 v1, 2, v0
	v_and_b32_e32 v1, 0xffffffc0, v1
	v_add_u32_e32 v1, s8, v1
	v_lshrrev_b32_e32 v130, 2, v0
	v_and_or_b32 v156, v130, 12, v1
	v_ashrrev_i32_e32 v157, 31, v156
	v_lshl_add_u64 v[150:151], v[156:157], 2, s[2:3]
	v_lshrrev_b32_e32 v254, 8, v0
	v_bfe_u32 v255, v0, 4, 2
	v_lshlrev_b32_e32 v254, 8, v254
	v_lshl_add_u32 v254, v255, 4, v254
	v_add_u32_e32 v254, 0x20000, v254
	ds_read_b128 v[138:141], v254
	ds_read_b128 v[142:145], v254 offset:64
	v_and_b32_e32 v130, 15, v0
	v_and_b32_e32 v180, 1, v0
	v_lshrrev_b32_e32 v0, 1, v0
	v_and_b32_e32 v131, 0x60, v0
	s_movk_i32 s3, 0xff6e
	v_lshl_or_b32 v131, s33, 8, v131
	v_lshlrev_b32_e32 v0, 4, v180
	v_or_b32_e32 v181, v131, v130
	v_bitop3_b32 v158, v131, s3, v130 bitop3:0xc8
	v_or_b32_e32 v130, v0, v156
	v_or_b32_e32 v132, 1, v181
	v_or_b32_e32 v134, 16, v158
	v_or_b32_e32 v136, 17, v181
	v_ashrrev_i32_e32 v131, 31, v130
	v_ashrrev_i32_e32 v133, 31, v132
	v_ashrrev_i32_e32 v135, 31, v134
	v_ashrrev_i32_e32 v137, 31, v136
	v_lshl_add_u64 v[160:161], v[130:131], 2, s[0:1]
	v_lshlrev_b64 v[152:153], 12, v[132:133]
	v_lshlrev_b64 v[148:149], 12, v[134:135]
	v_lshlrev_b64 v[146:147], 12, v[136:137]
	ds_read_b128 v[130:133], v254 offset:128
	ds_read_b128 v[134:137], v254 offset:192
	ds_read_b128 v[184:187], v254 offset:576
	ds_read_b128 v[188:191], v254 offset:512
	ds_read_b128 v[192:195], v254 offset:640
	ds_read_b128 v[196:199], v254 offset:704
	s_mov_b32 s2, 0x34800000
	v_cmp_eq_u32_e32 vcc, 0, v180
	v_mov_b32_e32 v173, 0
	v_mov_b32_e32 v174, 0
	v_mov_b32_e32 v175, 0
	v_ashrrev_i32_e32 v159, 31, v158
	v_mov_b32_e32 v176, 0
	v_mov_b32_e32 v177, 0
	v_mov_b32_e32 v178, 0
	v_mov_b32_e32 v179, 0
	v_lshlrev_b64 v[154:155], 12, v[158:159]
	v_lshl_add_u64 v[162:163], v[160:161], 0, v[154:155]
	v_lshl_add_u64 v[164:165], v[160:161], 0, v[152:153]
	v_lshl_add_u64 v[166:167], v[160:161], 0, v[148:149]
	v_mov_b32_e32 v1, 0
	s_waitcnt vmcnt(0) lgkmcnt(0)
	v_pk_fma_f32 v[128:129], v[128:129], s[2:3], v[140:141] op_sel_hi:[1,0,1]
	v_pk_fma_f32 v[126:127], v[126:127], s[2:3], v[138:139] op_sel_hi:[1,0,1]
	v_pk_fma_f32 v[120:121], v[120:121], s[2:3], v[144:145] op_sel_hi:[1,0,1]
	v_pk_fma_f32 v[118:119], v[118:119], s[2:3], v[142:143] op_sel_hi:[1,0,1]
	v_pk_fma_f32 v[124:125], v[124:125], s[2:3], v[140:141] op_sel_hi:[1,0,1]
	v_pk_fma_f32 v[122:123], v[122:123], s[2:3], v[138:139] op_sel_hi:[1,0,1]
	v_pk_fma_f32 v[168:169], v[116:117], s[2:3], v[144:145] op_sel_hi:[1,0,1]
	v_pk_fma_f32 v[170:171], v[114:115], s[2:3], v[142:143] op_sel_hi:[1,0,1]
	v_cndmask_b32_e32 v114, v129, v121, vcc
	v_cndmask_b32_e32 v115, v128, v120, vcc
	v_cndmask_b32_e32 v116, v127, v119, vcc
	v_cndmask_b32_e32 v117, v126, v118, vcc
	v_cndmask_b32_e32 v159, v125, v169, vcc
	v_cndmask_b32_e32 v180, v124, v168, vcc
	v_cndmask_b32_e32 v182, v123, v171, vcc
	v_cndmask_b32_e32 v183, v122, v170, vcc
	v_mov_b32_dpp v172, v117 quad_perm:[1,0,3,2] row_mask:0xf bank_mask:0xf
	v_mov_b32_dpp v173, v116 quad_perm:[1,0,3,2] row_mask:0xf bank_mask:0xf
	v_mov_b32_dpp v174, v115 quad_perm:[1,0,3,2] row_mask:0xf bank_mask:0xf
	v_mov_b32_dpp v175, v114 quad_perm:[1,0,3,2] row_mask:0xf bank_mask:0xf
	v_mov_b32_dpp v176, v183 quad_perm:[1,0,3,2] row_mask:0xf bank_mask:0xf
	v_mov_b32_dpp v177, v182 quad_perm:[1,0,3,2] row_mask:0xf bank_mask:0xf
	v_mov_b32_dpp v178, v180 quad_perm:[1,0,3,2] row_mask:0xf bank_mask:0xf
	v_mov_b32_dpp v179, v159 quad_perm:[1,0,3,2] row_mask:0xf bank_mask:0xf
	v_cndmask_b32_e32 v117, v175, v129, vcc
	v_cndmask_b32_e32 v116, v174, v128, vcc
	v_cndmask_b32_e32 v115, v173, v127, vcc
	v_cndmask_b32_e32 v114, v172, v126, vcc
	v_cndmask_b32_e32 v119, v119, v173, vcc
	v_pk_fma_f32 v[110:111], v[110:111], s[2:3], v[138:139] op_sel_hi:[1,0,1]
	v_pk_fma_f32 v[106:107], v[106:107], s[2:3], v[142:143] op_sel_hi:[1,0,1]
	v_cndmask_b32_e32 v121, v121, v175, vcc
	v_cndmask_b32_e32 v120, v120, v174, vcc
	v_cndmask_b32_e32 v118, v118, v172, vcc
	v_cndmask_b32_e32 v125, v179, v125, vcc
	v_cndmask_b32_e32 v124, v178, v124, vcc
	v_cndmask_b32_e32 v123, v177, v123, vcc
	v_cndmask_b32_e32 v122, v176, v122, vcc
	v_cndmask_b32_e32 v129, v169, v179, vcc
	v_cndmask_b32_e32 v128, v168, v178, vcc
	v_cndmask_b32_e32 v127, v171, v177, vcc
	v_cndmask_b32_e32 v126, v170, v176, vcc
	global_store_dwordx4 v[162:163], v[114:117], off sc1
	global_store_dwordx4 v[164:165], v[118:121], off sc1
	global_store_dwordx4 v[166:167], v[122:125], off sc1
	v_lshl_add_u64 v[114:115], v[160:161], 0, v[146:147]
	v_pk_fma_f32 v[112:113], v[112:113], s[2:3], v[140:141] op_sel_hi:[1,0,1]
	v_pk_fma_f32 v[108:109], v[108:109], s[2:3], v[144:145] op_sel_hi:[1,0,1]
	v_cndmask_b32_e32 v116, v111, v107, vcc
	v_mov_b32_e32 v119, 0
	global_store_dwordx4 v[114:115], v[126:129], off sc1
	v_cndmask_b32_e32 v115, v112, v108, vcc
	v_cndmask_b32_e32 v117, v110, v106, vcc
	v_mov_b32_e32 v118, 0
	v_mov_b32_dpp v119, v116 quad_perm:[1,0,3,2] row_mask:0xf bank_mask:0xf
	v_mov_b32_e32 v116, 0
	v_cndmask_b32_e32 v114, v113, v109, vcc
	v_mov_b32_dpp v118, v117 quad_perm:[1,0,3,2] row_mask:0xf bank_mask:0xf
	v_mov_b32_dpp v116, v115 quad_perm:[1,0,3,2] row_mask:0xf bank_mask:0xf
	v_mov_b32_e32 v115, 0
	v_cndmask_b32_e32 v112, v116, v112, vcc
	v_cndmask_b32_e32 v116, v108, v116, vcc
	v_mov_b32_dpp v115, v114 quad_perm:[1,0,3,2] row_mask:0xf bank_mask:0xf
	v_cndmask_b32_e32 v114, v106, v118, vcc
	v_or_b32_e32 v106, 0x80, v158
	v_cndmask_b32_e32 v113, v115, v113, vcc
	v_cndmask_b32_e32 v117, v109, v115, vcc
	v_cndmask_b32_e32 v115, v107, v119, vcc
	v_ashrrev_i32_e32 v107, 31, v106
	v_lshlrev_b64 v[108:109], 12, v[106:107]
	v_cndmask_b32_e32 v111, v119, v111, vcc
	v_cndmask_b32_e32 v110, v118, v110, vcc
	v_lshl_add_u64 v[106:107], v[160:161], 0, v[108:109]
	global_store_dwordx4 v[106:107], v[110:113], off sc1
	v_or_b32_e32 v106, 0x81, v181
	v_ashrrev_i32_e32 v107, 31, v106
	v_lshlrev_b64 v[106:107], 12, v[106:107]
	v_lshl_add_u64 v[110:111], v[160:161], 0, v[106:107]
	v_pk_fma_f32 v[102:103], v[102:103], s[2:3], v[138:139] op_sel_hi:[1,0,1]
	v_pk_fma_f32 v[98:99], v[98:99], s[2:3], v[142:143] op_sel_hi:[1,0,1]
	global_store_dwordx4 v[110:111], v[114:117], off sc1
	v_pk_fma_f32 v[104:105], v[104:105], s[2:3], v[140:141] op_sel_hi:[1,0,1]
	v_pk_fma_f32 v[100:101], v[100:101], s[2:3], v[144:145] op_sel_hi:[1,0,1]
	v_cndmask_b32_e32 v112, v103, v99, vcc
	v_mov_b32_e32 v115, 0
	v_cndmask_b32_e32 v111, v104, v100, vcc
	v_cndmask_b32_e32 v113, v102, v98, vcc
	v_mov_b32_e32 v114, 0
	v_mov_b32_dpp v115, v112 quad_perm:[1,0,3,2] row_mask:0xf bank_mask:0xf
	v_mov_b32_e32 v112, 0
	v_cndmask_b32_e32 v110, v105, v101, vcc
	v_mov_b32_dpp v114, v113 quad_perm:[1,0,3,2] row_mask:0xf bank_mask:0xf
	v_mov_b32_dpp v112, v111 quad_perm:[1,0,3,2] row_mask:0xf bank_mask:0xf
	v_mov_b32_e32 v111, 0
	v_cndmask_b32_e32 v104, v112, v104, vcc
	v_cndmask_b32_e32 v112, v100, v112, vcc
	v_mov_b32_dpp v111, v110 quad_perm:[1,0,3,2] row_mask:0xf bank_mask:0xf
	v_cndmask_b32_e32 v110, v98, v114, vcc
	v_or_b32_e32 v98, 0x90, v158
	v_cndmask_b32_e32 v105, v111, v105, vcc
	v_cndmask_b32_e32 v113, v101, v111, vcc
	v_cndmask_b32_e32 v111, v99, v115, vcc
	v_ashrrev_i32_e32 v99, 31, v98
	v_lshlrev_b64 v[100:101], 12, v[98:99]
	v_cndmask_b32_e32 v103, v115, v103, vcc
	v_cndmask_b32_e32 v102, v114, v102, vcc
	v_lshl_add_u64 v[98:99], v[160:161], 0, v[100:101]
	global_store_dwordx4 v[98:99], v[102:105], off sc1
	v_or_b32_e32 v98, 0x91, v181
	v_ashrrev_i32_e32 v99, 31, v98
	v_lshlrev_b64 v[98:99], 12, v[98:99]
	v_lshl_add_u64 v[102:103], v[160:161], 0, v[98:99]
	global_store_dwordx4 v[102:103], v[110:113], off sc1
	v_pk_fma_f32 v[96:97], v[96:97], s[2:3], v[132:133] op_sel_hi:[1,0,1]
	v_pk_fma_f32 v[94:95], v[94:95], s[2:3], v[130:131] op_sel_hi:[1,0,1]
	v_pk_fma_f32 v[104:105], v[92:93], s[2:3], v[136:137] op_sel_hi:[1,0,1]
	v_pk_fma_f32 v[110:111], v[90:91], s[2:3], v[134:135] op_sel_hi:[1,0,1]
	v_lshl_add_u64 v[102:103], v[0:1], 0, v[156:157]
	v_cndmask_b32_e32 v90, v97, v105, vcc
	v_cndmask_b32_e32 v91, v96, v104, vcc
	v_cndmask_b32_e32 v92, v95, v111, vcc
	v_cndmask_b32_e32 v93, v94, v110, vcc
	v_mov_b32_e32 v112, v1
	v_mov_b32_e32 v113, v1
	v_mov_b32_e32 v114, v1
	v_mov_b32_e32 v115, v1
	v_lshl_add_u64 v[102:103], v[102:103], 2, s[0:1]
	v_mov_b32_dpp v112, v93 quad_perm:[1,0,3,2] row_mask:0xf bank_mask:0xf
	v_mov_b32_dpp v113, v92 quad_perm:[1,0,3,2] row_mask:0xf bank_mask:0xf
	v_mov_b32_dpp v114, v91 quad_perm:[1,0,3,2] row_mask:0xf bank_mask:0xf
	v_mov_b32_dpp v115, v90 quad_perm:[1,0,3,2] row_mask:0xf bank_mask:0xf
	v_cndmask_b32_e32 v93, v115, v97, vcc
	v_cndmask_b32_e32 v92, v114, v96, vcc
	v_cndmask_b32_e32 v91, v113, v95, vcc
	v_cndmask_b32_e32 v90, v112, v94, vcc
	v_cndmask_b32_e32 v97, v105, v115, vcc
	v_cndmask_b32_e32 v96, v104, v114, vcc
	v_lshl_add_u64 v[104:105], v[102:103], 0, v[154:155]
	v_cndmask_b32_e32 v95, v111, v113, vcc
	v_cndmask_b32_e32 v94, v110, v112, vcc
	global_store_dwordx4 v[104:105], v[90:93], off offset:128 sc1
	v_pk_fma_f32 v[104:105], v[82:83], s[2:3], v[134:135] op_sel_hi:[1,0,1]
	v_mov_b32_e32 v111, v1
	v_lshl_add_u64 v[90:91], v[102:103], 0, v[152:153]
	global_store_dwordx4 v[90:91], v[94:97], off offset:128 sc1
	v_pk_fma_f32 v[90:91], v[88:89], s[2:3], v[132:133] op_sel_hi:[1,0,1]
	v_mov_b32_e32 v112, v1
	v_pk_fma_f32 v[94:95], v[86:87], s[2:3], v[130:131] op_sel_hi:[1,0,1]
	v_pk_fma_f32 v[96:97], v[84:85], s[2:3], v[136:137] op_sel_hi:[1,0,1]
	v_cndmask_b32_e32 v82, v94, v104, vcc
	s_nop 0
	v_cndmask_b32_e32 v110, v95, v105, vcc
	v_mov_b32_dpp v111, v82 quad_perm:[1,0,3,2] row_mask:0xf bank_mask:0xf
	s_nop 0
	v_cndmask_b32_e32 v92, v91, v97, vcc
	v_cndmask_b32_e32 v93, v90, v96, vcc
	v_mov_b32_dpp v112, v110 quad_perm:[1,0,3,2] row_mask:0xf bank_mask:0xf
	v_mov_b32_e32 v110, v1
	v_mov_b32_e32 v113, v1
	v_pk_fma_f32 v[80:81], v[80:81], s[2:3], v[132:133] op_sel_hi:[1,0,1]
	v_mov_b32_dpp v110, v93 quad_perm:[1,0,3,2] row_mask:0xf bank_mask:0xf
	v_mov_b32_dpp v113, v92 quad_perm:[1,0,3,2] row_mask:0xf bank_mask:0xf
	v_cndmask_b32_e32 v93, v113, v91, vcc
	v_cndmask_b32_e32 v92, v110, v90, vcc
	v_cndmask_b32_e32 v91, v112, v95, vcc
	v_cndmask_b32_e32 v90, v111, v94, vcc
	v_cndmask_b32_e32 v95, v105, v112, vcc
	v_cndmask_b32_e32 v94, v104, v111, vcc
	v_lshl_add_u64 v[104:105], v[102:103], 0, v[148:149]
	v_cndmask_b32_e32 v97, v97, v113, vcc
	v_cndmask_b32_e32 v96, v96, v110, vcc
	global_store_dwordx4 v[104:105], v[90:93], off offset:128 sc1
	v_pk_fma_f32 v[78:79], v[78:79], s[2:3], v[130:131] op_sel_hi:[1,0,1]
	v_pk_fma_f32 v[72:73], v[72:73], s[2:3], v[132:133] op_sel_hi:[1,0,1]
	v_lshl_add_u64 v[90:91], v[102:103], 0, v[146:147]
	global_store_dwordx4 v[90:91], v[94:97], off offset:128 sc1
	v_pk_fma_f32 v[90:91], v[76:77], s[2:3], v[136:137] op_sel_hi:[1,0,1]
	v_pk_fma_f32 v[92:93], v[74:75], s[2:3], v[134:135] op_sel_hi:[1,0,1]
	v_cndmask_b32_e32 v74, v81, v91, vcc
	v_cndmask_b32_e32 v75, v80, v90, vcc
	v_cndmask_b32_e32 v76, v79, v93, vcc
	v_cndmask_b32_e32 v77, v78, v92, vcc
	v_mov_b32_e32 v94, v1
	v_mov_b32_e32 v95, v1
	v_mov_b32_e32 v96, v1
	v_mov_b32_e32 v97, v1
	v_mov_b32_dpp v94, v77 quad_perm:[1,0,3,2] row_mask:0xf bank_mask:0xf
	v_mov_b32_dpp v95, v76 quad_perm:[1,0,3,2] row_mask:0xf bank_mask:0xf
	v_mov_b32_dpp v96, v75 quad_perm:[1,0,3,2] row_mask:0xf bank_mask:0xf
	v_mov_b32_dpp v97, v74 quad_perm:[1,0,3,2] row_mask:0xf bank_mask:0xf
	v_cndmask_b32_e32 v77, v97, v81, vcc
	v_cndmask_b32_e32 v76, v96, v80, vcc
	v_cndmask_b32_e32 v75, v95, v79, vcc
	v_cndmask_b32_e32 v74, v94, v78, vcc
	v_cndmask_b32_e32 v81, v91, v97, vcc
	v_cndmask_b32_e32 v80, v90, v96, vcc
	v_lshl_add_u64 v[90:91], v[102:103], 0, v[108:109]
	v_cndmask_b32_e32 v79, v93, v95, vcc
	v_cndmask_b32_e32 v78, v92, v94, vcc
	global_store_dwordx4 v[90:91], v[74:77], off offset:128 sc1
	v_pk_fma_f32 v[70:71], v[70:71], s[2:3], v[130:131] op_sel_hi:[1,0,1]
	s_nop 0
	v_pk_fma_f32 v[64:65], v[64:65], s[2:3], v[190:191] op_sel_hi:[1,0,1]
	v_lshl_add_u64 v[74:75], v[102:103], 0, v[106:107]
	global_store_dwordx4 v[74:75], v[78:81], off offset:128 sc1
	v_pk_fma_f32 v[74:75], v[68:69], s[2:3], v[136:137] op_sel_hi:[1,0,1]
	v_pk_fma_f32 v[76:77], v[66:67], s[2:3], v[134:135] op_sel_hi:[1,0,1]
	v_cndmask_b32_e32 v66, v73, v75, vcc
	v_cndmask_b32_e32 v67, v72, v74, vcc
	v_cndmask_b32_e32 v68, v71, v77, vcc
	v_cndmask_b32_e32 v69, v70, v76, vcc
	v_mov_b32_e32 v78, v1
	v_mov_b32_e32 v79, v1
	v_mov_b32_e32 v80, v1
	v_mov_b32_e32 v81, v1
	v_mov_b32_dpp v78, v69 quad_perm:[1,0,3,2] row_mask:0xf bank_mask:0xf
	v_mov_b32_dpp v79, v68 quad_perm:[1,0,3,2] row_mask:0xf bank_mask:0xf
	v_mov_b32_dpp v80, v67 quad_perm:[1,0,3,2] row_mask:0xf bank_mask:0xf
	v_mov_b32_dpp v81, v66 quad_perm:[1,0,3,2] row_mask:0xf bank_mask:0xf
	v_cndmask_b32_e32 v69, v81, v73, vcc
	v_cndmask_b32_e32 v68, v80, v72, vcc
	v_cndmask_b32_e32 v67, v79, v71, vcc
	v_cndmask_b32_e32 v66, v78, v70, vcc
	v_cndmask_b32_e32 v73, v75, v81, vcc
	v_cndmask_b32_e32 v72, v74, v80, vcc
	v_lshl_add_u64 v[74:75], v[102:103], 0, v[100:101]
	v_cndmask_b32_e32 v71, v77, v79, vcc
	v_cndmask_b32_e32 v70, v76, v78, vcc
	global_store_dwordx4 v[74:75], v[66:69], off offset:128 sc1
	v_pk_fma_f32 v[62:63], v[62:63], s[2:3], v[188:189] op_sel_hi:[1,0,1]
	v_mov_b32_e32 v74, v1
	v_lshl_add_u64 v[66:67], v[102:103], 0, v[98:99]
	global_store_dwordx4 v[66:67], v[70:73], off offset:128 sc1
	v_add_u32_e32 v66, 0x80, v156
	v_or_b32_e32 v68, v0, v66
	v_pk_fma_f32 v[70:71], v[60:61], s[2:3], v[186:187] op_sel_hi:[1,0,1]
	v_pk_fma_f32 v[72:73], v[58:59], s[2:3], v[184:185] op_sel_hi:[1,0,1]
	v_ashrrev_i32_e32 v69, 31, v68
	v_cndmask_b32_e32 v58, v65, v71, vcc
	v_cndmask_b32_e32 v59, v64, v70, vcc
	v_cndmask_b32_e32 v60, v63, v73, vcc
	v_cndmask_b32_e32 v61, v62, v72, vcc
	v_mov_b32_e32 v67, v1
	v_mov_b32_e32 v75, v1
	v_mov_b32_e32 v76, v1
	v_lshl_add_u64 v[68:69], v[68:69], 2, s[0:1]
	v_mov_b32_dpp v67, v61 quad_perm:[1,0,3,2] row_mask:0xf bank_mask:0xf
	v_mov_b32_dpp v74, v60 quad_perm:[1,0,3,2] row_mask:0xf bank_mask:0xf
	v_mov_b32_dpp v75, v59 quad_perm:[1,0,3,2] row_mask:0xf bank_mask:0xf
	v_mov_b32_dpp v76, v58 quad_perm:[1,0,3,2] row_mask:0xf bank_mask:0xf
	v_cndmask_b32_e32 v61, v76, v65, vcc
	v_cndmask_b32_e32 v60, v75, v64, vcc
	v_cndmask_b32_e32 v59, v74, v63, vcc
	v_cndmask_b32_e32 v58, v67, v62, vcc
	v_cndmask_b32_e32 v65, v71, v76, vcc
	v_cndmask_b32_e32 v64, v70, v75, vcc
	v_lshl_add_u64 v[70:71], v[68:69], 0, v[154:155]
	v_cndmask_b32_e32 v63, v73, v74, vcc
	v_cndmask_b32_e32 v62, v72, v67, vcc
	global_store_dwordx4 v[70:71], v[58:61], off sc1
	v_pk_fma_f32 v[70:71], v[50:51], s[2:3], v[184:185] op_sel_hi:[1,0,1]
	v_mov_b32_e32 v72, v1
	v_lshl_add_u64 v[58:59], v[68:69], 0, v[152:153]
	global_store_dwordx4 v[58:59], v[62:65], off sc1
	v_pk_fma_f32 v[58:59], v[56:57], s[2:3], v[190:191] op_sel_hi:[1,0,1]
	v_mov_b32_e32 v73, v1
	v_pk_fma_f32 v[62:63], v[54:55], s[2:3], v[188:189] op_sel_hi:[1,0,1]
	v_pk_fma_f32 v[64:65], v[52:53], s[2:3], v[186:187] op_sel_hi:[1,0,1]
	v_cndmask_b32_e32 v54, v62, v70, vcc
	s_nop 0
	v_cndmask_b32_e32 v67, v63, v71, vcc
	v_mov_b32_dpp v72, v54 quad_perm:[1,0,3,2] row_mask:0xf bank_mask:0xf
	s_nop 0
	v_cndmask_b32_e32 v60, v59, v65, vcc
	v_cndmask_b32_e32 v61, v58, v64, vcc
	v_mov_b32_dpp v73, v67 quad_perm:[1,0,3,2] row_mask:0xf bank_mask:0xf
	v_mov_b32_e32 v67, v1
	v_mov_b32_e32 v74, v1
	v_pk_fma_f32 v[48:49], v[48:49], s[2:3], v[190:191] op_sel_hi:[1,0,1]
	v_mov_b32_dpp v67, v61 quad_perm:[1,0,3,2] row_mask:0xf bank_mask:0xf
	v_mov_b32_dpp v74, v60 quad_perm:[1,0,3,2] row_mask:0xf bank_mask:0xf
	v_cndmask_b32_e32 v61, v74, v59, vcc
	v_cndmask_b32_e32 v60, v67, v58, vcc
	v_cndmask_b32_e32 v59, v73, v63, vcc
	v_cndmask_b32_e32 v58, v72, v62, vcc
	v_cndmask_b32_e32 v63, v71, v73, vcc
	v_cndmask_b32_e32 v62, v70, v72, vcc
	v_lshl_add_u64 v[70:71], v[68:69], 0, v[148:149]
	v_cndmask_b32_e32 v65, v65, v74, vcc
	v_cndmask_b32_e32 v64, v64, v67, vcc
	global_store_dwordx4 v[70:71], v[58:61], off sc1
	v_pk_fma_f32 v[46:47], v[46:47], s[2:3], v[188:189] op_sel_hi:[1,0,1]
	v_pk_fma_f32 v[40:41], v[40:41], s[2:3], v[190:191] op_sel_hi:[1,0,1]
	v_lshl_add_u64 v[58:59], v[68:69], 0, v[146:147]
	global_store_dwordx4 v[58:59], v[62:65], off sc1
	v_pk_fma_f32 v[58:59], v[44:45], s[2:3], v[186:187] op_sel_hi:[1,0,1]
	v_pk_fma_f32 v[60:61], v[42:43], s[2:3], v[184:185] op_sel_hi:[1,0,1]
	v_cndmask_b32_e32 v42, v49, v59, vcc
	v_cndmask_b32_e32 v43, v48, v58, vcc
	v_cndmask_b32_e32 v44, v47, v61, vcc
	v_cndmask_b32_e32 v45, v46, v60, vcc
	v_mov_b32_e32 v62, v1
	v_mov_b32_e32 v63, v1
	v_mov_b32_e32 v64, v1
	v_mov_b32_e32 v65, v1
	v_mov_b32_dpp v62, v45 quad_perm:[1,0,3,2] row_mask:0xf bank_mask:0xf
	v_mov_b32_dpp v63, v44 quad_perm:[1,0,3,2] row_mask:0xf bank_mask:0xf
	v_mov_b32_dpp v64, v43 quad_perm:[1,0,3,2] row_mask:0xf bank_mask:0xf
	v_mov_b32_dpp v65, v42 quad_perm:[1,0,3,2] row_mask:0xf bank_mask:0xf
	v_cndmask_b32_e32 v45, v65, v49, vcc
	v_cndmask_b32_e32 v44, v64, v48, vcc
	v_cndmask_b32_e32 v43, v63, v47, vcc
	v_cndmask_b32_e32 v42, v62, v46, vcc
	v_cndmask_b32_e32 v49, v59, v65, vcc
	v_cndmask_b32_e32 v48, v58, v64, vcc
	v_lshl_add_u64 v[58:59], v[68:69], 0, v[108:109]
	v_cndmask_b32_e32 v47, v61, v63, vcc
	v_cndmask_b32_e32 v46, v60, v62, vcc
	global_store_dwordx4 v[58:59], v[42:45], off sc1
	v_pk_fma_f32 v[38:39], v[38:39], s[2:3], v[188:189] op_sel_hi:[1,0,1]
	v_ashrrev_i32_e32 v67, 31, v66
	v_lshl_add_u64 v[42:43], v[68:69], 0, v[106:107]
	global_store_dwordx4 v[42:43], v[46:49], off sc1
	v_pk_fma_f32 v[42:43], v[32:33], s[2:3], v[186:187] op_sel_hi:[1,0,1]
	v_pk_fma_f32 v[44:45], v[30:31], s[2:3], v[184:185] op_sel_hi:[1,0,1]
	v_cndmask_b32_e32 v30, v41, v43, vcc
	v_cndmask_b32_e32 v31, v40, v42, vcc
	v_cndmask_b32_e32 v32, v39, v45, vcc
	v_cndmask_b32_e32 v33, v38, v44, vcc
	v_mov_b32_e32 v46, v1
	v_mov_b32_e32 v47, v1
	v_mov_b32_e32 v48, v1
	v_mov_b32_e32 v49, v1
	v_mov_b32_dpp v46, v33 quad_perm:[1,0,3,2] row_mask:0xf bank_mask:0xf
	v_mov_b32_dpp v47, v32 quad_perm:[1,0,3,2] row_mask:0xf bank_mask:0xf
	v_mov_b32_dpp v48, v31 quad_perm:[1,0,3,2] row_mask:0xf bank_mask:0xf
	v_mov_b32_dpp v49, v30 quad_perm:[1,0,3,2] row_mask:0xf bank_mask:0xf
	v_cndmask_b32_e32 v33, v49, v41, vcc
	v_cndmask_b32_e32 v32, v48, v40, vcc
	v_cndmask_b32_e32 v31, v47, v39, vcc
	v_cndmask_b32_e32 v30, v46, v38, vcc
	v_cndmask_b32_e32 v41, v43, v49, vcc
	v_cndmask_b32_e32 v40, v42, v48, vcc
	v_lshl_add_u64 v[42:43], v[68:69], 0, v[100:101]
	v_cndmask_b32_e32 v39, v45, v47, vcc
	v_cndmask_b32_e32 v38, v44, v46, vcc
	global_store_dwordx4 v[42:43], v[30:33], off sc1
	v_mov_b32_e32 v42, v1
	v_mov_b32_e32 v43, v1
	v_lshl_add_u64 v[30:31], v[68:69], 0, v[98:99]
	global_store_dwordx4 v[30:31], v[38:41], off sc1
	v_lshl_add_u64 v[30:31], v[0:1], 0, v[66:67]
	s_nop 0
	v_pk_fma_f32 v[32:33], v[34:35], s[2:3], v[192:193] op_sel_hi:[1,0,1]
	v_lshl_add_u64 v[38:39], v[30:31], 2, s[0:1]
	v_pk_fma_f32 v[30:31], v[36:37], s[2:3], v[194:195] op_sel_hi:[1,0,1]
	v_pk_fma_f32 v[34:35], v[28:29], s[2:3], v[198:199] op_sel_hi:[1,0,1]
	v_pk_fma_f32 v[36:37], v[26:27], s[2:3], v[196:197] op_sel_hi:[1,0,1]
	v_cndmask_b32_e32 v0, v31, v35, vcc
	v_cndmask_b32_e32 v26, v30, v34, vcc
	v_cndmask_b32_e32 v27, v33, v37, vcc
	v_cndmask_b32_e32 v28, v32, v36, vcc
	v_mov_b32_e32 v40, v1
	v_mov_b32_e32 v41, v1
	v_mov_b32_dpp v42, v26 quad_perm:[1,0,3,2] row_mask:0xf bank_mask:0xf
	v_mov_b32_dpp v40, v28 quad_perm:[1,0,3,2] row_mask:0xf bank_mask:0xf
	v_mov_b32_dpp v41, v27 quad_perm:[1,0,3,2] row_mask:0xf bank_mask:0xf
	v_mov_b32_dpp v43, v0 quad_perm:[1,0,3,2] row_mask:0xf bank_mask:0xf
	v_cndmask_b32_e32 v29, v43, v31, vcc
	v_cndmask_b32_e32 v28, v42, v30, vcc
	v_cndmask_b32_e32 v27, v41, v33, vcc
	v_cndmask_b32_e32 v26, v40, v32, vcc
	v_cndmask_b32_e32 v33, v35, v43, vcc
	v_cndmask_b32_e32 v32, v34, v42, vcc
	v_lshl_add_u64 v[34:35], v[38:39], 0, v[154:155]
	v_cndmask_b32_e32 v31, v37, v41, vcc
	v_cndmask_b32_e32 v30, v36, v40, vcc
	global_store_dwordx4 v[34:35], v[26:29], off offset:128 sc1
	v_pk_fma_f32 v[24:25], v[24:25], s[2:3], v[194:195] op_sel_hi:[1,0,1]
	v_pk_fma_f32 v[22:23], v[22:23], s[2:3], v[192:193] op_sel_hi:[1,0,1]
	v_lshl_add_u64 v[26:27], v[38:39], 0, v[152:153]
	global_store_dwordx4 v[26:27], v[30:33], off offset:128 sc1
	v_pk_fma_f32 v[26:27], v[20:21], s[2:3], v[198:199] op_sel_hi:[1,0,1]
	v_pk_fma_f32 v[28:29], v[18:19], s[2:3], v[196:197] op_sel_hi:[1,0,1]
	v_cndmask_b32_e32 v0, v25, v27, vcc
	v_cndmask_b32_e32 v18, v24, v26, vcc
	v_cndmask_b32_e32 v19, v23, v29, vcc
	v_cndmask_b32_e32 v20, v22, v28, vcc
	v_mov_b32_e32 v30, v1
	v_mov_b32_e32 v31, v1
	v_mov_b32_e32 v32, v1
	v_mov_b32_e32 v33, v1
	v_mov_b32_dpp v30, v20 quad_perm:[1,0,3,2] row_mask:0xf bank_mask:0xf
	v_mov_b32_dpp v31, v19 quad_perm:[1,0,3,2] row_mask:0xf bank_mask:0xf
	v_mov_b32_dpp v32, v18 quad_perm:[1,0,3,2] row_mask:0xf bank_mask:0xf
	v_mov_b32_dpp v33, v0 quad_perm:[1,0,3,2] row_mask:0xf bank_mask:0xf
	v_cndmask_b32_e32 v21, v33, v25, vcc
	v_cndmask_b32_e32 v20, v32, v24, vcc
	v_cndmask_b32_e32 v19, v31, v23, vcc
	v_cndmask_b32_e32 v18, v30, v22, vcc
	v_cndmask_b32_e32 v25, v27, v33, vcc
	v_cndmask_b32_e32 v24, v26, v32, vcc
	v_lshl_add_u64 v[26:27], v[38:39], 0, v[148:149]
	v_cndmask_b32_e32 v23, v29, v31, vcc
	v_cndmask_b32_e32 v22, v28, v30, vcc
	global_store_dwordx4 v[26:27], v[18:21], off offset:128 sc1
	v_pk_fma_f32 v[16:17], v[16:17], s[2:3], v[194:195] op_sel_hi:[1,0,1]
	v_pk_fma_f32 v[14:15], v[14:15], s[2:3], v[192:193] op_sel_hi:[1,0,1]
	v_lshl_add_u64 v[18:19], v[38:39], 0, v[146:147]
	global_store_dwordx4 v[18:19], v[22:25], off offset:128 sc1
	v_pk_fma_f32 v[18:19], v[12:13], s[2:3], v[198:199] op_sel_hi:[1,0,1]
	v_pk_fma_f32 v[20:21], v[10:11], s[2:3], v[196:197] op_sel_hi:[1,0,1]
	v_cndmask_b32_e32 v0, v17, v19, vcc
	v_cndmask_b32_e32 v10, v16, v18, vcc
	v_cndmask_b32_e32 v11, v15, v21, vcc
	v_cndmask_b32_e32 v12, v14, v20, vcc
	v_mov_b32_e32 v22, v1
	v_mov_b32_e32 v23, v1
	v_mov_b32_e32 v24, v1
	v_mov_b32_e32 v25, v1
	v_mov_b32_dpp v22, v12 quad_perm:[1,0,3,2] row_mask:0xf bank_mask:0xf
	v_mov_b32_dpp v23, v11 quad_perm:[1,0,3,2] row_mask:0xf bank_mask:0xf
	v_mov_b32_dpp v24, v10 quad_perm:[1,0,3,2] row_mask:0xf bank_mask:0xf
	v_mov_b32_dpp v25, v0 quad_perm:[1,0,3,2] row_mask:0xf bank_mask:0xf
	v_cndmask_b32_e32 v13, v25, v17, vcc
	v_cndmask_b32_e32 v12, v24, v16, vcc
	v_cndmask_b32_e32 v11, v23, v15, vcc
	v_cndmask_b32_e32 v10, v22, v14, vcc
	v_cndmask_b32_e32 v17, v19, v25, vcc
	v_cndmask_b32_e32 v16, v18, v24, vcc
	v_lshl_add_u64 v[18:19], v[38:39], 0, v[108:109]
	v_cndmask_b32_e32 v15, v21, v23, vcc
	v_cndmask_b32_e32 v14, v20, v22, vcc
	global_store_dwordx4 v[18:19], v[10:13], off offset:128 sc1
	v_pk_fma_f32 v[8:9], v[8:9], s[2:3], v[194:195] op_sel_hi:[1,0,1]
	v_pk_fma_f32 v[6:7], v[6:7], s[2:3], v[192:193] op_sel_hi:[1,0,1]
	v_lshl_add_u64 v[10:11], v[38:39], 0, v[106:107]
	global_store_dwordx4 v[10:11], v[14:17], off offset:128 sc1
	v_pk_fma_f32 v[10:11], v[4:5], s[2:3], v[198:199] op_sel_hi:[1,0,1]
	v_pk_fma_f32 v[12:13], v[2:3], s[2:3], v[196:197] op_sel_hi:[1,0,1]
	v_cndmask_b32_e32 v0, v9, v11, vcc
	v_cndmask_b32_e32 v2, v8, v10, vcc
	v_cndmask_b32_e32 v3, v7, v13, vcc
	v_cndmask_b32_e32 v4, v6, v12, vcc
	v_mov_b32_e32 v14, v1
	v_mov_b32_e32 v15, v1
	v_mov_b32_e32 v16, v1
	v_mov_b32_dpp v14, v4 quad_perm:[1,0,3,2] row_mask:0xf bank_mask:0xf
	v_mov_b32_dpp v15, v3 quad_perm:[1,0,3,2] row_mask:0xf bank_mask:0xf
	v_mov_b32_dpp v16, v2 quad_perm:[1,0,3,2] row_mask:0xf bank_mask:0xf
	v_mov_b32_dpp v1, v0 quad_perm:[1,0,3,2] row_mask:0xf bank_mask:0xf
	v_cndmask_b32_e32 v5, v1, v9, vcc
	v_cndmask_b32_e32 v4, v16, v8, vcc
	v_cndmask_b32_e32 v3, v15, v7, vcc
	v_cndmask_b32_e32 v2, v14, v6, vcc
	v_cndmask_b32_e32 v9, v11, v1, vcc
	v_lshl_add_u64 v[0:1], v[38:39], 0, v[100:101]
	v_cndmask_b32_e32 v8, v10, v16, vcc
	v_cndmask_b32_e32 v7, v13, v15, vcc
	v_cndmask_b32_e32 v6, v12, v14, vcc
	global_store_dwordx4 v[0:1], v[2:5], off offset:128 sc1
	v_lshl_add_u64 v[0:1], v[38:39], 0, v[98:99]
	global_store_dwordx4 v[0:1], v[6:9], off offset:128 sc1
	s_endpgm
